# speedup vs baseline: 1.0041x; 1.0041x over previous
.LBB1_9:
	v_add_u32_e32 v182, s20, v209
	ds_read_b64_tr_b16 v[178:179], v182 offset:24576
	ds_read_b64_tr_b16 v[180:181], v182 offset:25088
	s_waitcnt lgkmcnt(9)
	v_mfma_f32_32x32x16_f16 v[98:113], v[174:177], v[142:145], v[34:49]
	v_add_f32_e32 v82, v66, v67
	v_add_f32_e32 v82, v68, v82
	v_add_f32_e32 v82, v69, v82
	v_add_f32_e32 v82, v70, v82
	v_add_f32_e32 v82, v71, v82
	v_cvt_pk_f16_f32 v134, v66, v67
	v_cvt_pk_f16_f32 v135, v68, v69
	ds_read_b64_tr_b16 v[174:175], v182 offset:28672
	ds_read_b64_tr_b16 v[176:177], v182 offset:29184
	v_add_f32_e32 v66, v72, v82
	s_waitcnt lgkmcnt(10)
	v_mfma_f32_32x32x16_f16 v[82:97], v[170:173], v[142:145], v[34:49]
	v_add_f32_e32 v66, v73, v66
	v_add_f32_e32 v66, v74, v66
	v_add_f32_e32 v66, v75, v66
	v_cvt_pk_f16_f32 v136, v70, v71
	v_cvt_pk_f16_f32 v137, v72, v73
	ds_read_b64_tr_b16 v[170:171], v182 offset:25600
	ds_read_b64_tr_b16 v[172:173], v182 offset:26112
	s_waitcnt lgkmcnt(11)
	v_mfma_f32_32x32x16_f16 v[98:113], v[166:169], v[138:141], v[98:113]
	v_add_f32_e32 v66, v76, v66
	v_add_f32_e32 v66, v77, v66
	v_add_f32_e32 v66, v78, v66
	v_add_f32_e32 v66, v79, v66
	v_cvt_pk_f16_f32 v126, v74, v75
	v_cvt_pk_f16_f32 v127, v76, v77
	ds_read_b64_tr_b16 v[74:75], v182 offset:29696
	ds_read_b64_tr_b16 v[76:77], v182 offset:30208
	s_waitcnt lgkmcnt(12)
	v_mfma_f32_32x32x16_f16 v[82:97], v[162:165], v[138:141], v[82:97]
	v_add_f32_e32 v66, v80, v66
	v_add_f32_e32 v66, v81, v66
	v_add_f32_e32 v66, v50, v66
	v_add_f32_e32 v66, v51, v66
	v_cvt_pk_f16_f32 v128, v78, v79
	v_cvt_pk_f16_f32 v129, v80, v81
	ds_read_b64_tr_b16 v[70:71], v182 offset:26624
	ds_read_b64_tr_b16 v[72:73], v182 offset:27136
	s_waitcnt lgkmcnt(13)
	v_mfma_f32_32x32x16_f16 v[98:113], v[158:161], v[130:133], v[98:113]
	v_add_f32_e32 v66, v52, v66
	v_add_f32_e32 v66, v53, v66
	v_add_f32_e32 v66, v54, v66
	v_add_f32_e32 v78, v55, v66
	v_cvt_pk_f16_f32 v118, v50, v51
	v_cvt_pk_f16_f32 v119, v52, v53
	ds_read_b64_tr_b16 v[66:67], v182 offset:30720
	ds_read_b64_tr_b16 v[68:69], v182 offset:31232
	s_waitcnt lgkmcnt(14)
	v_mfma_f32_32x32x16_f16 v[82:97], v[154:157], v[130:133], v[82:97]
	v_add_f32_e32 v50, v56, v78
	v_add_f32_e32 v50, v57, v50
	v_add_f32_e32 v50, v58, v50
	v_add_f32_e32 v50, v59, v50
	v_cvt_pk_f16_f32 v120, v54, v55
	v_cvt_pk_f16_f32 v121, v56, v57
	ds_read_b64_tr_b16 v[54:55], v182 offset:27648
	ds_read_b64_tr_b16 v[56:57], v182 offset:28160
	s_waitcnt lgkmcnt(14)
	v_mfma_f32_32x32x16_f16 v[98:113], v[150:153], v[122:125], v[98:113]
	v_add_f32_e32 v50, v60, v50
	v_add_f32_e32 v50, v61, v50
	v_add_f32_e32 v50, v62, v50
	v_add_f32_e32 v78, v63, v50
	v_cvt_pk_f16_f32 v114, v58, v59
	v_cvt_pk_f16_f32 v115, v60, v61
	ds_read_b64_tr_b16 v[50:51], v182 offset:31744
	ds_read_b64_tr_b16 v[52:53], v182 offset:32256
	v_mfma_f32_32x32x16_f16 v[82:97], v[146:149], v[122:125], v[82:97]
	v_add_f32_e32 v58, v64, v78
	v_add_f32_e32 v58, v65, v58
	v_cvt_pk_f16_f32 v116, v62, v63
	v_cvt_pk_f16_f32 v117, v64, v65
	v_max_f32_e32 v59, v98, v99
	v_max3_f32 v60, v100, v101, v102
	v_max3_f32 v59, v59, v103, v104
	v_max3_f32 v60, v60, v105, v106
	v_max3_f32 v59, v59, v107, v108
	v_max3_f32 v60, v60, v109, v110
	v_max3_f32 v59, v59, v111, v112
	v_add_f32_e32 v182, v203, v58
	v_max3_f32 v60, v60, v113, v82
	v_max3_f32 v59, v59, v83, v84
	v_max3_f32 v60, v60, v85, v86
	v_max3_f32 v59, v59, v87, v88
	v_max3_f32 v60, v60, v89, v90
	v_max3_f32 v59, v59, v91, v92
	v_max3_f32 v60, v60, v93, v94
	v_max3_f32 v59, v59, v95, v96
	v_max3_f32 v58, v59, v60, v97
	v_mov_b32_e32 v59, v58
	s_add_u32 s52, s16, 0xffffe000
	s_addc_u32 s53, s17, -1
	v_permlane32_swap_b32_e32 v58, v59
	v_max_f32_e32 v58, v58, v59
	v_cmp_lt_f32_e32 vcc, s23, v58
	s_cmp_lg_u64 vcc, 0
	s_cselect_b64 s[2:3], -1, 0
	s_cbranch_vccnz .LBB1_17
.LBB1_10:
	s_waitcnt lgkmcnt(14)
	v_mfma_f32_32x32x16_f16 v[2:17], v[134:137], v[178:181], v[2:17]
	v_exp_f32_e32 v98, v98
	v_exp_f32_e32 v99, v99
	v_exp_f32_e32 v100, v100
	v_exp_f32_e32 v101, v101
	s_add_i32 s54, s24, s39
	s_mov_b32 m0, s54
	s_waitcnt lgkmcnt(12)
	v_mfma_f32_32x32x16_f16 v[18:33], v[134:137], v[174:177], v[18:33]
	global_load_lds_dwordx4 v211, s[52:53]
	v_exp_f32_e32 v102, v102
	v_exp_f32_e32 v103, v103
	v_exp_f32_e32 v104, v104
	v_exp_f32_e32 v105, v105
	v_add_u32_e32 v62, s22, v200
	ds_read_b128 v[58:61], v62
	ds_read_b128 v[146:149], v62 offset:512
	s_add_i32 s54, s22, s40
	s_mov_b32 m0, s54
	s_waitcnt lgkmcnt(12)
	v_mfma_f32_32x32x16_f16 v[2:17], v[126:129], v[170:173], v[2:17]
	global_load_lds_dwordx4 v211, s[18:19]
	v_exp_f32_e32 v106, v106
	v_exp_f32_e32 v107, v107
	v_exp_f32_e32 v108, v108
	v_exp_f32_e32 v109, v109
	ds_read_b128 v[178:181], v62 offset:2048
	ds_read_b128 v[170:173], v62 offset:2560
	s_waitcnt lgkmcnt(12)
	v_mfma_f32_32x32x16_f16 v[18:33], v[126:129], v[74:77], v[18:33]
	v_exp_f32_e32 v110, v110
	v_exp_f32_e32 v111, v111
	v_exp_f32_e32 v112, v112
	v_exp_f32_e32 v113, v113
	ds_read_b128 v[174:177], v62 offset:4096
	ds_read_b128 v[162:165], v62 offset:4608
	s_waitcnt lgkmcnt(12)
	v_mfma_f32_32x32x16_f16 v[2:17], v[118:121], v[70:73], v[2:17]
	v_exp_f32_e32 v82, v82
	v_exp_f32_e32 v83, v83
	v_exp_f32_e32 v84, v84
	v_exp_f32_e32 v85, v85
	ds_read_b128 v[166:169], v62 offset:6144
	ds_read_b128 v[158:161], v62 offset:6656
	s_waitcnt lgkmcnt(12)
	v_mfma_f32_32x32x16_f16 v[18:33], v[118:121], v[66:69], v[18:33]
	v_exp_f32_e32 v86, v86
	v_exp_f32_e32 v87, v87
	v_exp_f32_e32 v88, v88
	v_exp_f32_e32 v89, v89
	s_waitcnt lgkmcnt(10)
	v_mfma_f32_32x32x16_f16 v[2:17], v[114:117], v[54:57], v[2:17]
	v_exp_f32_e32 v90, v90
	v_exp_f32_e32 v91, v91
	v_exp_f32_e32 v92, v92
	v_exp_f32_e32 v93, v93
	s_waitcnt lgkmcnt(8)
	v_mfma_f32_32x32x16_f16 v[18:33], v[114:117], v[50:53], v[18:33]
	v_exp_f32_e32 v94, v94
	v_exp_f32_e32 v95, v95
	v_exp_f32_e32 v96, v96
	v_exp_f32_e32 v97, v97
	s_waitcnt vmcnt(2) lgkmcnt(0)
	s_barrier
	s_andn2_b64 vcc, exec, s[2:3]
	v_add_u32_e32 v202, s38, v212
	s_cbranch_vccnz .LBB1_12
	s_waitcnt lgkmcnt(0)
	ds_read_b128 v[50:53], v202 offset:49248
	ds_read_b128 v[54:57], v202 offset:49216
	ds_read_b128 v[62:65], v202 offset:49184
	ds_read_b128 v[66:69], v202 offset:49152
	s_waitcnt lgkmcnt(3)
	v_pk_mul_f32 v[14:15], v[14:15], v[50:51]
	s_waitcnt lgkmcnt(2)
	v_pk_mul_f32 v[10:11], v[10:11], v[54:55]
	s_waitcnt lgkmcnt(1)
	v_pk_mul_f32 v[6:7], v[6:7], v[62:63]
	v_pk_mul_f32 v[16:17], v[16:17], v[52:53]
	v_pk_mul_f32 v[12:13], v[12:13], v[56:57]
	v_pk_mul_f32 v[8:9], v[8:9], v[64:65]
	s_waitcnt lgkmcnt(0)
	v_pk_mul_f32 v[4:5], v[4:5], v[68:69]
	v_pk_mul_f32 v[2:3], v[2:3], v[66:67]
	v_pk_mul_f32 v[30:31], v[30:31], v[50:51]
	v_pk_mul_f32 v[26:27], v[26:27], v[54:55]
	v_pk_mul_f32 v[22:23], v[22:23], v[62:63]
	v_pk_mul_f32 v[32:33], v[32:33], v[52:53]
	v_pk_mul_f32 v[28:29], v[28:29], v[56:57]
	v_pk_mul_f32 v[24:25], v[24:25], v[64:65]
	v_pk_mul_f32 v[20:21], v[20:21], v[68:69]
	v_pk_mul_f32 v[18:19], v[18:19], v[66:67]
.LBB1_12:
	s_add_i32 s2, s22, 0x2000
	s_cmpk_lg_i32 s22, 0x4000
	s_cselect_b32 s43, s2, 0
	v_add_u32_e32 v183, s24, v209
	ds_read_b64_tr_b16 v[154:155], v183 offset:24576
	ds_read_b64_tr_b16 v[156:157], v183 offset:25088
	s_waitcnt lgkmcnt(9)
	v_mfma_f32_32x32x16_f16 v[66:81], v[58:61], v[142:145], v[34:49]
	v_add_f32_e32 v50, v98, v99
	v_add_f32_e32 v50, v100, v50
	v_add_f32_e32 v50, v101, v50
	v_add_f32_e32 v50, v102, v50
	v_add_f32_e32 v50, v103, v50
	v_cvt_pk_f16_f32 v134, v98, v99
	v_cvt_pk_f16_f32 v135, v100, v101
	ds_read_b64_tr_b16 v[150:151], v183 offset:28672
	ds_read_b64_tr_b16 v[152:153], v183 offset:29184
	v_add_f32_e32 v50, v104, v50
	v_add_f32_e32 v50, v105, v50
	v_add_f32_e32 v50, v106, v50
	v_add_f32_e32 v98, v107, v50
	s_waitcnt lgkmcnt(10)
	v_mfma_f32_32x32x16_f16 v[50:65], v[146:149], v[142:145], v[34:49]
	v_cvt_pk_f16_f32 v136, v102, v103
	v_cvt_pk_f16_f32 v137, v104, v105
	ds_read_b64_tr_b16 v[146:147], v183 offset:25600
	ds_read_b64_tr_b16 v[148:149], v183 offset:26112
	s_waitcnt lgkmcnt(11)
	v_mfma_f32_32x32x16_f16 v[66:81], v[178:181], v[138:141], v[66:81]
	v_add_f32_e32 v98, v108, v98
	v_add_f32_e32 v98, v109, v98
	v_add_f32_e32 v98, v110, v98
	v_add_f32_e32 v98, v111, v98
	v_cvt_pk_f16_f32 v126, v106, v107
	v_cvt_pk_f16_f32 v127, v108, v109
	ds_read_b64_tr_b16 v[106:107], v183 offset:29696
	ds_read_b64_tr_b16 v[108:109], v183 offset:30208
	s_waitcnt lgkmcnt(12)
	v_mfma_f32_32x32x16_f16 v[50:65], v[170:173], v[138:141], v[50:65]
	v_add_f32_e32 v98, v112, v98
	v_add_f32_e32 v98, v113, v98
	v_add_f32_e32 v98, v82, v98
	v_add_f32_e32 v98, v83, v98
	v_cvt_pk_f16_f32 v128, v110, v111
	v_cvt_pk_f16_f32 v129, v112, v113
	ds_read_b64_tr_b16 v[102:103], v183 offset:26624
	ds_read_b64_tr_b16 v[104:105], v183 offset:27136
	s_waitcnt lgkmcnt(13)
	v_mfma_f32_32x32x16_f16 v[66:81], v[174:177], v[130:133], v[66:81]
	v_add_f32_e32 v98, v84, v98
	v_add_f32_e32 v98, v85, v98
	v_add_f32_e32 v98, v86, v98
	v_add_f32_e32 v110, v87, v98
	v_cvt_pk_f16_f32 v118, v82, v83
	v_cvt_pk_f16_f32 v119, v84, v85
	ds_read_b64_tr_b16 v[98:99], v183 offset:30720
	ds_read_b64_tr_b16 v[100:101], v183 offset:31232
	s_waitcnt lgkmcnt(14)
	v_mfma_f32_32x32x16_f16 v[50:65], v[162:165], v[130:133], v[50:65]
	v_add_f32_e32 v82, v88, v110
	v_add_f32_e32 v82, v89, v82
	v_add_f32_e32 v82, v90, v82
	v_add_f32_e32 v82, v91, v82
	v_cvt_pk_f16_f32 v120, v86, v87
	v_cvt_pk_f16_f32 v121, v88, v89
	ds_read_b64_tr_b16 v[86:87], v183 offset:27648
	ds_read_b64_tr_b16 v[88:89], v183 offset:28160
	s_waitcnt lgkmcnt(14)
	v_mfma_f32_32x32x16_f16 v[66:81], v[166:169], v[122:125], v[66:81]
	v_add_f32_e32 v82, v92, v82
	v_add_f32_e32 v82, v93, v82
	v_add_f32_e32 v82, v94, v82
	v_add_f32_e32 v110, v95, v82
	v_cvt_pk_f16_f32 v114, v90, v91
	v_cvt_pk_f16_f32 v115, v92, v93
	ds_read_b64_tr_b16 v[82:83], v183 offset:31744
	ds_read_b64_tr_b16 v[84:85], v183 offset:32256
	v_mfma_f32_32x32x16_f16 v[50:65], v[158:161], v[122:125], v[50:65]
	v_add_f32_e32 v90, v96, v110
	v_add_f32_e32 v90, v97, v90
	v_cvt_pk_f16_f32 v116, v94, v95
	v_cvt_pk_f16_f32 v117, v96, v97
	v_max_f32_e32 v91, v66, v67
	v_max3_f32 v92, v68, v69, v70
	v_max3_f32 v91, v91, v71, v72
	v_max3_f32 v92, v92, v73, v74
	v_max3_f32 v91, v91, v75, v76
	v_max3_f32 v92, v92, v77, v78
	v_max3_f32 v91, v91, v79, v80
	v_add_f32_e32 v203, v182, v90
	v_max3_f32 v92, v92, v81, v50
	v_max3_f32 v91, v91, v51, v52
	v_max3_f32 v92, v92, v53, v54
	v_max3_f32 v91, v91, v55, v56
	v_max3_f32 v92, v92, v57, v58
	v_max3_f32 v91, v91, v59, v60
	v_max3_f32 v92, v92, v61, v62
	v_max3_f32 v91, v91, v63, v64
	v_max3_f32 v90, v91, v92, v65
	v_mov_b32_e32 v91, v90
	s_add_u32 s52, s18, 0x2000
	s_addc_u32 s53, s19, 0
	v_permlane32_swap_b32_e32 v90, v91
	v_max_f32_e32 v90, v90, v91
	v_cmp_lt_f32_e32 vcc, s23, v90
	s_cmp_lg_u64 vcc, 0
	s_cselect_b64 s[2:3], -1, 0
	s_cbranch_vccnz .LBB1_20
.LBB1_13:
	s_waitcnt lgkmcnt(14)
	v_mfma_f32_32x32x16_f16 v[2:17], v[134:137], v[154:157], v[2:17]
	v_exp_f32_e32 v66, v66
	v_exp_f32_e32 v67, v67
	v_exp_f32_e32 v68, v68
	v_exp_f32_e32 v69, v69
	s_add_i32 s54, s22, s39
	s_mov_b32 m0, s54
	s_waitcnt lgkmcnt(12)
	v_mfma_f32_32x32x16_f16 v[18:33], v[134:137], v[150:153], v[18:33]
	global_load_lds_dwordx4 v211, s[16:17]
	v_exp_f32_e32 v70, v70
	v_exp_f32_e32 v71, v71
	v_exp_f32_e32 v72, v72
	v_exp_f32_e32 v73, v73
	v_add_u32_e32 v90, s43, v200
	ds_read_b128 v[174:177], v90
	ds_read_b128 v[170:173], v90 offset:512
	s_add_i32 s54, s43, s40
	s_mov_b32 m0, s54
	s_waitcnt lgkmcnt(12)
	v_mfma_f32_32x32x16_f16 v[2:17], v[126:129], v[146:149], v[2:17]
	global_load_lds_dwordx4 v211, s[52:53]
	v_exp_f32_e32 v74, v74
	v_exp_f32_e32 v75, v75
	v_exp_f32_e32 v76, v76
	v_exp_f32_e32 v77, v77
	ds_read_b128 v[166:169], v90 offset:2048
	ds_read_b128 v[162:165], v90 offset:2560
	s_waitcnt lgkmcnt(12)
	v_mfma_f32_32x32x16_f16 v[18:33], v[126:129], v[106:109], v[18:33]
	v_exp_f32_e32 v78, v78
	v_exp_f32_e32 v79, v79
	v_exp_f32_e32 v80, v80
	v_exp_f32_e32 v81, v81
	ds_read_b128 v[158:161], v90 offset:4096
	ds_read_b128 v[154:157], v90 offset:4608
	s_waitcnt lgkmcnt(12)
	v_mfma_f32_32x32x16_f16 v[2:17], v[118:121], v[102:105], v[2:17]
	v_exp_f32_e32 v50, v50
	v_exp_f32_e32 v51, v51
	v_exp_f32_e32 v52, v52
	v_exp_f32_e32 v53, v53
	ds_read_b128 v[150:153], v90 offset:6144
	ds_read_b128 v[146:149], v90 offset:6656
	s_waitcnt lgkmcnt(12)
	v_mfma_f32_32x32x16_f16 v[18:33], v[118:121], v[98:101], v[18:33]
	v_exp_f32_e32 v54, v54
	v_exp_f32_e32 v55, v55
	v_exp_f32_e32 v56, v56
	v_exp_f32_e32 v57, v57
	s_waitcnt lgkmcnt(10)
	v_mfma_f32_32x32x16_f16 v[2:17], v[114:117], v[86:89], v[2:17]
	v_exp_f32_e32 v58, v58
	v_exp_f32_e32 v59, v59
	v_exp_f32_e32 v60, v60
	v_exp_f32_e32 v61, v61
	s_waitcnt lgkmcnt(8)
	v_mfma_f32_32x32x16_f16 v[18:33], v[114:117], v[82:85], v[18:33]
	v_exp_f32_e32 v62, v62
	v_exp_f32_e32 v63, v63
	v_exp_f32_e32 v64, v64
	v_exp_f32_e32 v65, v65
	s_waitcnt vmcnt(2) lgkmcnt(0)
	s_barrier
	s_andn2_b64 vcc, exec, s[2:3]
	s_cbranch_vccnz .LBB1_15
	s_waitcnt lgkmcnt(0)
	ds_read_b128 v[82:85], v202 offset:49248
	ds_read_b128 v[86:89], v202 offset:49216
	ds_read_b128 v[90:93], v202 offset:49184
	ds_read_b128 v[94:97], v202 offset:49152
	s_waitcnt lgkmcnt(3)
	v_pk_mul_f32 v[14:15], v[14:15], v[82:83]
	s_waitcnt lgkmcnt(2)
	v_pk_mul_f32 v[10:11], v[10:11], v[86:87]
	s_waitcnt lgkmcnt(1)
	v_pk_mul_f32 v[6:7], v[6:7], v[90:91]
	v_pk_mul_f32 v[16:17], v[16:17], v[84:85]
	v_pk_mul_f32 v[12:13], v[12:13], v[88:89]
	v_pk_mul_f32 v[8:9], v[8:9], v[92:93]
	s_waitcnt lgkmcnt(0)
	v_pk_mul_f32 v[4:5], v[4:5], v[96:97]
	v_pk_mul_f32 v[2:3], v[2:3], v[94:95]
	v_pk_mul_f32 v[30:31], v[30:31], v[82:83]
	v_pk_mul_f32 v[26:27], v[26:27], v[86:87]
	v_pk_mul_f32 v[22:23], v[22:23], v[90:91]
	v_pk_mul_f32 v[32:33], v[32:33], v[84:85]
	v_pk_mul_f32 v[28:29], v[28:29], v[88:89]
	v_pk_mul_f32 v[24:25], v[24:25], v[92:93]
	v_pk_mul_f32 v[20:21], v[20:21], v[96:97]
	v_pk_mul_f32 v[18:19], v[18:19], v[94:95]

.LBB1_87:
	v_add_u32_e32 v65, s6, v251
	ds_read_b64_tr_b16 v[192:193], v65
	ds_read_b64_tr_b16 v[194:195], v65 offset:512
	s_waitcnt lgkmcnt(9)
	v_mfma_f32_32x32x16_f16 v[112:127], v[188:191], v[140:143], v[32:47]
	v_add_f32_e32 v66, v80, v81
	v_add_f32_e32 v66, v82, v66
	v_add_f32_e32 v66, v83, v66
	v_add_f32_e32 v66, v84, v66
	v_add_f32_e32 v66, v85, v66
	v_cvt_pk_f16_f32 v156, v80, v81
	v_cvt_pk_f16_f32 v157, v82, v83
	ds_read_b64_tr_b16 v[188:189], v65 offset:4096
	ds_read_b64_tr_b16 v[190:191], v65 offset:4608
	s_waitcnt lgkmcnt(10)
	v_mfma_f32_32x32x16_f16 v[96:111], v[184:187], v[140:143], v[32:47]
	v_add_f32_e32 v66, v86, v66
	v_add_f32_e32 v66, v87, v66
	v_add_f32_e32 v66, v88, v66
	v_add_f32_e32 v66, v89, v66
	v_cvt_pk_f16_f32 v158, v84, v85
	v_cvt_pk_f16_f32 v159, v86, v87
	ds_read_b64_tr_b16 v[78:79], v65 offset:1024
	ds_read_b64_tr_b16 v[80:81], v65 offset:1536
	s_waitcnt lgkmcnt(11)
	v_mfma_f32_32x32x16_f16 v[112:127], v[180:183], v[136:139], v[112:127]
	v_add_f32_e32 v66, v90, v66
	v_add_f32_e32 v66, v91, v66
	v_add_f32_e32 v66, v92, v66
	v_add_f32_e32 v66, v93, v66
	v_cvt_pk_f16_f32 v152, v88, v89
	v_cvt_pk_f16_f32 v153, v90, v91
	ds_read_b64_tr_b16 v[74:75], v65 offset:5120
	ds_read_b64_tr_b16 v[76:77], v65 offset:5632
	s_waitcnt lgkmcnt(12)
	v_mfma_f32_32x32x16_f16 v[96:111], v[176:179], v[136:139], v[96:111]
	v_add_f32_e32 v66, v94, v66
	v_add_f32_e32 v66, v95, v66
	v_add_f32_e32 v66, v48, v66
	v_add_f32_e32 v66, v49, v66
	v_cvt_pk_f16_f32 v154, v92, v93
	v_cvt_pk_f16_f32 v155, v94, v95
	ds_read_b64_tr_b16 v[70:71], v65 offset:2048
	ds_read_b64_tr_b16 v[72:73], v65 offset:2560
	s_waitcnt lgkmcnt(13)
	v_mfma_f32_32x32x16_f16 v[112:127], v[172:175], v[132:135], v[112:127]
	v_add_f32_e32 v66, v50, v66
	v_add_f32_e32 v66, v51, v66
	v_add_f32_e32 v66, v52, v66
	v_add_f32_e32 v82, v53, v66
	v_cvt_pk_f16_f32 v148, v48, v49
	v_cvt_pk_f16_f32 v149, v50, v51
	ds_read_b64_tr_b16 v[66:67], v65 offset:6144
	ds_read_b64_tr_b16 v[68:69], v65 offset:6656
	s_waitcnt lgkmcnt(14)
	v_mfma_f32_32x32x16_f16 v[96:111], v[168:171], v[132:135], v[96:111]
	v_add_f32_e32 v48, v54, v82
	v_add_f32_e32 v48, v55, v48
	v_add_f32_e32 v48, v56, v48
	v_add_f32_e32 v48, v57, v48
	v_cvt_pk_f16_f32 v150, v52, v53
	v_cvt_pk_f16_f32 v151, v54, v55
	ds_read_b64_tr_b16 v[52:53], v65 offset:3072
	ds_read_b64_tr_b16 v[54:55], v65 offset:3584
	s_waitcnt lgkmcnt(14)
	v_mfma_f32_32x32x16_f16 v[112:127], v[164:167], v[128:131], v[112:127]
	v_add_f32_e32 v48, v58, v48
	v_add_f32_e32 v48, v59, v48
	v_add_f32_e32 v48, v60, v48
	v_add_f32_e32 v82, v61, v48
	v_cvt_pk_f16_f32 v144, v56, v57
	v_cvt_pk_f16_f32 v145, v58, v59
	ds_read_b64_tr_b16 v[48:49], v65 offset:7168
	ds_read_b64_tr_b16 v[50:51], v65 offset:7680
	v_mfma_f32_32x32x16_f16 v[96:111], v[160:163], v[128:131], v[96:111]
	v_add_f32_e32 v56, v62, v82
	v_add_f32_e32 v56, v63, v56
	v_cvt_pk_f16_f32 v146, v60, v61
	v_cvt_pk_f16_f32 v147, v62, v63
	v_max_f32_e32 v57, v112, v113
	v_max3_f32 v58, v114, v115, v116
	v_max3_f32 v57, v57, v117, v118
	v_max3_f32 v58, v58, v119, v120
	v_max3_f32 v57, v57, v121, v122
	v_max3_f32 v58, v58, v123, v124
	v_max3_f32 v57, v57, v125, v126
	v_add_f32_e32 v64, v64, v56
	v_max3_f32 v58, v58, v127, v96
	v_max3_f32 v57, v57, v97, v98
	v_max3_f32 v58, v58, v99, v100
	v_max3_f32 v57, v57, v101, v102
	v_max3_f32 v58, v58, v103, v104
	v_max3_f32 v57, v57, v105, v106
	v_max3_f32 v58, v58, v107, v108
	v_max3_f32 v57, v57, v109, v110
	v_max3_f32 v56, v57, v58, v111
	v_mov_b32_e32 v57, v56
	s_add_u32 s52, s4, 0xffffe000
	s_addc_u32 s53, s5, -1
	v_permlane32_swap_b32_e32 v56, v57
	v_max_f32_e32 v56, v56, v57
	v_cmp_lt_f32_e32 vcc, s17, v56
	s_cmp_lg_u64 vcc, 0
	s_cselect_b64 s[6:7], -1, 0
	s_cbranch_vccnz .LBB1_95
.LBB1_88:
	s_waitcnt lgkmcnt(14)
	v_mfma_f32_32x32x16_f16 v[0:15], v[156:159], v[192:195], v[0:15]
	v_exp_f32_e32 v112, v112
	v_exp_f32_e32 v113, v113
	v_exp_f32_e32 v114, v114
	v_exp_f32_e32 v115, v115
	s_add_i32 s54, s30, s22
	s_mov_b32 m0, s54
	s_waitcnt lgkmcnt(12)
	v_mfma_f32_32x32x16_f16 v[16:31], v[156:159], v[188:191], v[16:31]
	global_load_lds_dwordx4 v211, s[52:53]
	v_exp_f32_e32 v116, v116
	v_exp_f32_e32 v117, v117
	v_exp_f32_e32 v118, v118
	v_exp_f32_e32 v119, v119
	v_add_u32_e32 v60, s12, v250
	ds_read_b128 v[56:59], v60
	ds_read_b128 v[160:163], v60 offset:512
	s_add_u32 s52, s2, 0xffffe000
	s_addc_u32 s53, s3, -1
	s_add_i32 s54, s12, s23
	s_mov_b32 m0, s54
	s_waitcnt lgkmcnt(12)
	v_mfma_f32_32x32x16_f16 v[0:15], v[152:155], v[78:81], v[0:15]
	global_load_lds_dwordx4 v211, s[52:53]
	v_exp_f32_e32 v120, v120
	v_exp_f32_e32 v121, v121
	v_exp_f32_e32 v122, v122
	v_exp_f32_e32 v123, v123
	ds_read_b128 v[188:191], v60 offset:2048
	ds_read_b128 v[184:187], v60 offset:2560
	s_waitcnt lgkmcnt(12)
	v_mfma_f32_32x32x16_f16 v[16:31], v[152:155], v[74:77], v[16:31]
	v_exp_f32_e32 v124, v124
	v_exp_f32_e32 v125, v125
	v_exp_f32_e32 v126, v126
	v_exp_f32_e32 v127, v127
	ds_read_b128 v[74:77], v60 offset:4096
	ds_read_b128 v[176:179], v60 offset:4608
	s_waitcnt lgkmcnt(12)
	v_mfma_f32_32x32x16_f16 v[0:15], v[148:151], v[70:73], v[0:15]
	v_exp_f32_e32 v96, v96
	v_exp_f32_e32 v97, v97
	v_exp_f32_e32 v98, v98
	v_exp_f32_e32 v99, v99
	ds_read_b128 v[180:183], v60 offset:6144
	ds_read_b128 v[172:175], v60 offset:6656
	s_waitcnt lgkmcnt(12)
	v_mfma_f32_32x32x16_f16 v[16:31], v[148:151], v[66:69], v[16:31]
	v_exp_f32_e32 v100, v100
	v_exp_f32_e32 v101, v101
	v_exp_f32_e32 v102, v102
	v_exp_f32_e32 v103, v103
	s_waitcnt lgkmcnt(10)
	v_mfma_f32_32x32x16_f16 v[0:15], v[144:147], v[52:55], v[0:15]
	v_exp_f32_e32 v104, v104
	v_exp_f32_e32 v105, v105
	v_exp_f32_e32 v106, v106
	v_exp_f32_e32 v107, v107
	s_waitcnt lgkmcnt(8)
	v_mfma_f32_32x32x16_f16 v[16:31], v[144:147], v[48:51], v[16:31]
	v_exp_f32_e32 v108, v108
	v_exp_f32_e32 v109, v109
	v_exp_f32_e32 v110, v110
	v_exp_f32_e32 v111, v111
	s_waitcnt vmcnt(2) lgkmcnt(0)
	s_barrier
	s_andn2_b64 vcc, exec, s[6:7]
	s_cbranch_vccnz .LBB1_90
	s_waitcnt lgkmcnt(0)
	v_add_u32_e32 v65, s21, v212
	ds_read_b128 v[48:51], v65 offset:49248
	ds_read_b128 v[52:55], v65 offset:49216
	ds_read_b128 v[60:63], v65 offset:49184
	ds_read_b128 v[66:69], v65 offset:49152
	s_waitcnt lgkmcnt(3)
	v_pk_mul_f32 v[12:13], v[12:13], v[48:49]
	s_waitcnt lgkmcnt(2)
	v_pk_mul_f32 v[8:9], v[8:9], v[52:53]
	s_waitcnt lgkmcnt(1)
	v_pk_mul_f32 v[4:5], v[4:5], v[60:61]
	v_pk_mul_f32 v[14:15], v[14:15], v[50:51]
	v_pk_mul_f32 v[10:11], v[10:11], v[54:55]
	v_pk_mul_f32 v[6:7], v[6:7], v[62:63]
	s_waitcnt lgkmcnt(0)
	v_pk_mul_f32 v[2:3], v[2:3], v[68:69]
	v_pk_mul_f32 v[0:1], v[0:1], v[66:67]
	v_pk_mul_f32 v[28:29], v[28:29], v[48:49]
	v_pk_mul_f32 v[24:25], v[24:25], v[52:53]
	v_pk_mul_f32 v[20:21], v[20:21], v[60:61]
	v_pk_mul_f32 v[30:31], v[30:31], v[50:51]
	v_pk_mul_f32 v[26:27], v[26:27], v[54:55]
	v_pk_mul_f32 v[22:23], v[22:23], v[62:63]
	v_pk_mul_f32 v[18:19], v[18:19], v[68:69]
	v_pk_mul_f32 v[16:17], v[16:17], v[66:67]
.LBB1_90:
	s_add_i32 s6, s12, 0x2000
	s_cmpk_lg_i32 s12, 0x4000
	s_cselect_b32 s25, s6, 0
	v_add_u32_e32 v65, s30, v251
	ds_read_b64_tr_b16 v[168:169], v65
	ds_read_b64_tr_b16 v[170:171], v65 offset:512
	s_waitcnt lgkmcnt(9)
	v_mfma_f32_32x32x16_f16 v[80:95], v[56:59], v[140:143], v[32:47]
	v_add_f32_e32 v48, v112, v113
	v_add_f32_e32 v48, v114, v48
	v_add_f32_e32 v48, v115, v48
	v_add_f32_e32 v48, v116, v48
	v_add_f32_e32 v48, v117, v48
	v_cvt_pk_f16_f32 v156, v112, v113
	v_cvt_pk_f16_f32 v157, v114, v115
	ds_read_b64_tr_b16 v[164:165], v65 offset:4096
	ds_read_b64_tr_b16 v[166:167], v65 offset:4608
	v_add_f32_e32 v48, v118, v48
	v_add_f32_e32 v48, v119, v48
	v_add_f32_e32 v48, v120, v48
	v_add_f32_e32 v66, v121, v48
	s_waitcnt lgkmcnt(10)
	v_mfma_f32_32x32x16_f16 v[48:63], v[160:163], v[140:143], v[32:47]
	v_cvt_pk_f16_f32 v158, v116, v117
	v_cvt_pk_f16_f32 v159, v118, v119
	ds_read_b64_tr_b16 v[160:161], v65 offset:1024
	ds_read_b64_tr_b16 v[162:163], v65 offset:1536
	s_waitcnt lgkmcnt(11)
	v_mfma_f32_32x32x16_f16 v[80:95], v[188:191], v[136:139], v[80:95]
	v_add_f32_e32 v66, v122, v66
	v_add_f32_e32 v66, v123, v66
	v_add_f32_e32 v66, v124, v66
	v_add_f32_e32 v66, v125, v66
	v_cvt_pk_f16_f32 v152, v120, v121
	v_cvt_pk_f16_f32 v153, v122, v123
	ds_read_b64_tr_b16 v[116:117], v65 offset:5120
	ds_read_b64_tr_b16 v[118:119], v65 offset:5632
	s_waitcnt lgkmcnt(12)
	v_mfma_f32_32x32x16_f16 v[48:63], v[184:187], v[136:139], v[48:63]
	v_add_f32_e32 v66, v126, v66
	v_add_f32_e32 v66, v127, v66
	v_add_f32_e32 v66, v96, v66
	v_add_f32_e32 v66, v97, v66
	v_cvt_pk_f16_f32 v154, v124, v125
	v_cvt_pk_f16_f32 v155, v126, v127
	ds_read_b64_tr_b16 v[112:113], v65 offset:2048
	ds_read_b64_tr_b16 v[114:115], v65 offset:2560
	s_waitcnt lgkmcnt(13)
	v_mfma_f32_32x32x16_f16 v[80:95], v[74:77], v[132:135], v[80:95]
	v_add_f32_e32 v66, v98, v66
	v_add_f32_e32 v66, v99, v66
	v_add_f32_e32 v66, v100, v66
	v_add_f32_e32 v66, v101, v66
	v_cvt_pk_f16_f32 v148, v96, v97
	v_cvt_pk_f16_f32 v149, v98, v99
	ds_read_b64_tr_b16 v[74:75], v65 offset:6144
	ds_read_b64_tr_b16 v[76:77], v65 offset:6656
	s_waitcnt lgkmcnt(14)
	v_mfma_f32_32x32x16_f16 v[48:63], v[176:179], v[132:135], v[48:63]
	v_add_f32_e32 v66, v102, v66
	v_add_f32_e32 v66, v103, v66
	v_add_f32_e32 v66, v104, v66
	v_add_f32_e32 v66, v105, v66
	v_cvt_pk_f16_f32 v150, v100, v101
	v_cvt_pk_f16_f32 v151, v102, v103
	ds_read_b64_tr_b16 v[70:71], v65 offset:3072
	ds_read_b64_tr_b16 v[72:73], v65 offset:3584
	s_waitcnt lgkmcnt(14)
	v_mfma_f32_32x32x16_f16 v[80:95], v[180:183], v[128:131], v[80:95]
	v_add_f32_e32 v66, v106, v66
	v_add_f32_e32 v66, v107, v66
	v_add_f32_e32 v66, v108, v66
	v_add_f32_e32 v78, v109, v66
	v_cvt_pk_f16_f32 v144, v104, v105
	v_cvt_pk_f16_f32 v145, v106, v107
	ds_read_b64_tr_b16 v[66:67], v65 offset:7168
	ds_read_b64_tr_b16 v[68:69], v65 offset:7680
	v_mfma_f32_32x32x16_f16 v[48:63], v[172:175], v[128:131], v[48:63]
	v_add_f32_e32 v65, v110, v78
	v_add_f32_e32 v65, v111, v65
	v_cvt_pk_f16_f32 v146, v108, v109
	v_cvt_pk_f16_f32 v147, v110, v111
	v_max_f32_e32 v78, v80, v81
	v_max3_f32 v79, v82, v83, v84
	v_max3_f32 v78, v78, v85, v86
	v_max3_f32 v79, v79, v87, v88
	v_max3_f32 v78, v78, v89, v90
	v_max3_f32 v79, v79, v91, v92
	v_max3_f32 v78, v78, v93, v94
	v_add_f32_e32 v64, v64, v65
	v_max3_f32 v79, v79, v95, v48
	v_max3_f32 v78, v78, v49, v50
	v_max3_f32 v79, v79, v51, v52
	v_max3_f32 v78, v78, v53, v54
	v_max3_f32 v79, v79, v55, v56
	v_max3_f32 v78, v78, v57, v58
	v_max3_f32 v79, v79, v59, v60
	v_max3_f32 v78, v78, v61, v62
	v_max3_f32 v65, v78, v79, v63
	v_mov_b32_e32 v78, v65
	s_add_i32 s54, s12, s22
	s_add_i32 s55, s25, s23
	v_permlane32_swap_b32_e32 v65, v78
	v_max_f32_e32 v65, v65, v78
	v_cmp_lt_f32_e32 vcc, s17, v65
	s_cmp_lg_u64 vcc, 0
	s_cselect_b64 s[6:7], -1, 0
	s_cbranch_vccnz .LBB1_98
.LBB1_91:
	s_waitcnt lgkmcnt(14)
	v_mfma_f32_32x32x16_f16 v[0:15], v[156:159], v[168:171], v[0:15]
	v_exp_f32_e32 v80, v80
	v_exp_f32_e32 v81, v81
	v_exp_f32_e32 v82, v82
	v_exp_f32_e32 v83, v83
	s_mov_b32 m0, s54
	s_waitcnt lgkmcnt(12)
	v_mfma_f32_32x32x16_f16 v[16:31], v[156:159], v[164:167], v[16:31]
	global_load_lds_dwordx4 v211, s[4:5]
	v_exp_f32_e32 v84, v84
	v_exp_f32_e32 v85, v85
	v_exp_f32_e32 v86, v86
	v_exp_f32_e32 v87, v87
	v_add_u32_e32 v65, s25, v250
	ds_read_b128 v[188:191], v65
	ds_read_b128 v[184:187], v65 offset:512
	s_mov_b32 m0, s55
	s_waitcnt lgkmcnt(12)
	v_mfma_f32_32x32x16_f16 v[0:15], v[152:155], v[160:163], v[0:15]
	global_load_lds_dwordx4 v211, s[2:3]
	v_exp_f32_e32 v88, v88
	v_exp_f32_e32 v89, v89
	v_exp_f32_e32 v90, v90
	v_exp_f32_e32 v91, v91
	ds_read_b128 v[180:183], v65 offset:2048
	ds_read_b128 v[176:179], v65 offset:2560
	s_waitcnt lgkmcnt(12)
	v_mfma_f32_32x32x16_f16 v[16:31], v[152:155], v[116:119], v[16:31]
	v_exp_f32_e32 v92, v92
	v_exp_f32_e32 v93, v93
	v_exp_f32_e32 v94, v94
	v_exp_f32_e32 v95, v95
	ds_read_b128 v[172:175], v65 offset:4096
	ds_read_b128 v[168:171], v65 offset:4608
	s_waitcnt lgkmcnt(12)
	v_mfma_f32_32x32x16_f16 v[0:15], v[148:151], v[112:115], v[0:15]
	v_exp_f32_e32 v48, v48
	v_exp_f32_e32 v49, v49
	v_exp_f32_e32 v50, v50
	v_exp_f32_e32 v51, v51
	ds_read_b128 v[164:167], v65 offset:6144
	ds_read_b128 v[160:163], v65 offset:6656
	s_waitcnt lgkmcnt(12)
	v_mfma_f32_32x32x16_f16 v[16:31], v[148:151], v[74:77], v[16:31]
	v_exp_f32_e32 v52, v52
	v_exp_f32_e32 v53, v53
	v_exp_f32_e32 v54, v54
	v_exp_f32_e32 v55, v55
	s_waitcnt lgkmcnt(10)
	v_mfma_f32_32x32x16_f16 v[0:15], v[144:147], v[70:73], v[0:15]
	v_exp_f32_e32 v56, v56
	v_exp_f32_e32 v57, v57
	v_exp_f32_e32 v58, v58
	v_exp_f32_e32 v59, v59
	s_waitcnt lgkmcnt(8)
	v_mfma_f32_32x32x16_f16 v[16:31], v[144:147], v[66:69], v[16:31]
	v_exp_f32_e32 v60, v60
	v_exp_f32_e32 v61, v61
	v_exp_f32_e32 v62, v62
	v_exp_f32_e32 v63, v63
	s_waitcnt vmcnt(2) lgkmcnt(0)
	s_barrier
	s_andn2_b64 vcc, exec, s[6:7]
	s_cbranch_vccnz .LBB1_93
	s_waitcnt lgkmcnt(0)
	v_add_u32_e32 v65, s21, v212
	ds_read_b128 v[66:69], v65 offset:49248
	ds_read_b128 v[70:73], v65 offset:49216
	ds_read_b128 v[74:77], v65 offset:49184
	ds_read_b128 v[96:99], v65 offset:49152
	s_waitcnt lgkmcnt(3)
	v_pk_mul_f32 v[12:13], v[12:13], v[66:67]
	s_waitcnt lgkmcnt(2)
	v_pk_mul_f32 v[8:9], v[8:9], v[70:71]
	s_waitcnt lgkmcnt(1)
	v_pk_mul_f32 v[4:5], v[4:5], v[74:75]
	v_pk_mul_f32 v[14:15], v[14:15], v[68:69]
	v_pk_mul_f32 v[10:11], v[10:11], v[72:73]
	v_pk_mul_f32 v[6:7], v[6:7], v[76:77]
	s_waitcnt lgkmcnt(0)
	v_pk_mul_f32 v[2:3], v[2:3], v[98:99]
	v_pk_mul_f32 v[0:1], v[0:1], v[96:97]
	v_pk_mul_f32 v[28:29], v[28:29], v[66:67]
	v_pk_mul_f32 v[24:25], v[24:25], v[70:71]
	v_pk_mul_f32 v[20:21], v[20:21], v[74:75]
	v_pk_mul_f32 v[30:31], v[30:31], v[68:69]
	v_pk_mul_f32 v[26:27], v[26:27], v[72:73]
	v_pk_mul_f32 v[22:23], v[22:23], v[76:77]
	v_pk_mul_f32 v[18:19], v[18:19], v[98:99]
	v_pk_mul_f32 v[16:17], v[16:17], v[96:97]
